# phase 1: upper half of the grid converts its static w_gu share before its in-projection units (phase re-dispatch), so one half streams HBM while the other half runs GEMM
# speedup vs baseline: 1.0333x; 1.0194x over previous
_Z7enc_fwd4Args:
	v_and_b32_e32 v1, 0x3ff, v0
	v_writelane_b32 v253, s2, 0
	s_load_dwordx2 s[2:3], s[0:1], 0xa0
	s_load_dword s76, s[0:1], 0xa8
	v_mbcnt_lo_u32_b32 v2, -1, 0
	v_mbcnt_hi_u32_b32 v2, -1, v2
	s_waitcnt lgkmcnt(0)
	v_writelane_b32 v253, s2, 1
	s_nop 1
	v_writelane_b32 v253, s3, 2
	v_readfirstlane_b32 s3, v1
	s_and_b32 s4, s3, 0xffffffc0
	v_writelane_b32 v253, s4, 3
	v_add_u32_e32 v2, s4, v2
	s_add_u32 s4, s0, 0xa8
	v_writelane_b32 v253, s0, 4
	s_addc_u32 s5, s1, 0
	s_mov_b32 s2, 0
	s_mov_b32 s100, 0
	v_writelane_b32 v253, s1, 5
	v_writelane_b32 v253, s4, 6
	v_cmp_gt_i32_e32 vcc, 2, v2
	s_nop 0
	v_writelane_b32 v253, s5, 7
	s_and_saveexec_b64 s[0:1], vcc
	v_lshl_add_u32 v3, v2, 2, 0
	v_add_u32_e32 v3, 0x20040, v3
	v_mov_b32_e32 v4, 0
	ds_write_b32 v3, v4
	s_or_b64 exec, exec, s[0:1]
	v_readlane_b32 s0, v253, 1
	v_readlane_b32 s1, v253, 2
	s_sub_i32 s0, s1, s0
	s_cmp_lt_i32 s0, 2
	s_waitcnt lgkmcnt(0)
	s_barrier
	s_cbranch_scc1 .LBB0_7
	s_getreg_b32 s0, hwreg(HW_REG_XCC_ID, 0, 4)
	s_and_b32 s2, s0, 15
	v_cmp_eq_u32_e32 vcc, 0, v2
	s_and_saveexec_b64 s[0:1], vcc
	s_cbranch_execz .LBB0_6
	s_mov_b64 s[4:5], exec
	v_mbcnt_lo_u32_b32 v2, s4, 0
	v_mbcnt_hi_u32_b32 v2, s5, v2
	v_cmp_eq_u32_e32 vcc, 0, v2
	s_and_b64 s[6:7], exec, vcc
	s_mov_b64 exec, s[6:7]
	s_cbranch_execz .LBB0_6
	v_readlane_b32 s6, v253, 4
	v_readlane_b32 s7, v253, 5
	s_load_dwordx2 s[6:7], s[6:7], 0x98
	s_lshl_b32 s8, s2, 8
	v_mov_b32_e32 v2, 0x4000
	s_waitcnt lgkmcnt(0)
	s_add_u32 s6, s6, s8
	s_addc_u32 s7, s7, 0
	s_bcnt1_i32_b64 s4, s[4:5]
	v_mov_b32_e32 v3, s4
	global_atomic_add v2, v3, s[6:7] offset:1024

.LBB0_554:
	ds_read_b128 v[50:53], v244 offset:16384
	s_add_i32 s4, s4, 4
	v_cmp_lt_i32_e32 vcc, 26, v249
	v_cmp_lt_i32_e64 s[40:41], -1, v249
	v_cmp_lt_i32_e64 s[42:43], 0, v249
	v_cmp_lt_i32_e64 s[44:45], 1, v249
	v_cmp_lt_i32_e64 s[46:47], 2, v249
	v_cmp_lt_i32_e64 s[48:49], 7, v249
	v_cmp_lt_i32_e64 s[50:51], 8, v249
	s_waitcnt lgkmcnt(0)
	v_mfma_f32_32x32x16_bf16 v[50:65], v[50:53], v[142:145], 0
	ds_read_b128 v[142:145], v245 offset:16384
	v_cmp_lt_i32_e64 s[52:53], 9, v249
	v_cmp_lt_i32_e64 s[54:55], 10, v249
	v_cmp_lt_i32_e64 s[56:57], 15, v249
	v_cmp_lt_i32_e64 s[58:59], 16, v249
	v_cmp_lt_i32_e64 s[60:61], 17, v249
	v_cmp_lt_i32_e64 s[62:63], 18, v249
	v_cmp_lt_i32_e64 s[64:65], 23, v249
	s_waitcnt lgkmcnt(0)
	v_mfma_f32_32x32x16_bf16 v[50:65], v[142:145], v[138:141], v[50:65]
	ds_read_b128 v[138:141], v246 offset:16384
	ds_read_b128 v[142:145], v247 offset:16384
	v_cmp_lt_i32_e64 s[66:67], 24, v249
	s_cmp_lt_i32 s4, s94
	v_cmp_lt_i32_e64 s[68:69], 25, v249
	s_waitcnt lgkmcnt(1)
	v_mfma_f32_32x32x16_bf16 v[50:65], v[138:141], v[134:137], v[50:65]
	s_waitcnt lgkmcnt(0)
	v_mfma_f32_32x32x16_bf16 v[50:65], v[142:145], v[130:133], v[50:65]
	s_cbranch_scc1 .LBB0_556
	v_mov_b32_e32 v136, 0xf149f2ca
	v_mov_b32_e32 v137, v136
	v_mov_b32_e32 v134, v136
	v_mov_b32_e32 v135, v136
	v_mov_b32_e32 v132, v136
	v_mov_b32_e32 v133, v136
	v_mov_b32_e32 v130, v136
	v_mov_b32_e32 v131, v136
	s_nop 2
	v_mov_b32_e32 v56, v136
	v_mov_b32_e32 v57, v136
	v_mov_b32_e32 v54, v136
	v_mov_b32_e32 v55, v136
	v_mov_b32_e32 v52, v136
	v_mov_b32_e32 v53, v136
	v_mov_b32_e32 v64, v136
	v_mov_b32_e32 v65, v136
	s_branch .LBB0_557
.Les_tramp:
	s_branch .LBB0_13
.LBB0_556:
	s_nop 10
	v_cndmask_b32_e32 v65, v228, v65, vcc
	v_cndmask_b32_e64 v136, v228, v50, s[40:41]
	v_cndmask_b32_e64 v137, v228, v51, s[42:43]
	v_cndmask_b32_e64 v134, v228, v52, s[44:45]
	v_cndmask_b32_e64 v135, v228, v53, s[46:47]
	v_cndmask_b32_e64 v132, v228, v54, s[48:49]
	v_cndmask_b32_e64 v133, v228, v55, s[50:51]
	v_cndmask_b32_e64 v130, v228, v56, s[52:53]
	v_cndmask_b32_e64 v131, v228, v57, s[54:55]
	v_cndmask_b32_e64 v56, v228, v58, s[56:57]
	v_cndmask_b32_e64 v57, v228, v59, s[58:59]
	v_cndmask_b32_e64 v54, v228, v60, s[60:61]
	v_cndmask_b32_e64 v55, v228, v61, s[62:63]
	v_cndmask_b32_e64 v52, v228, v62, s[64:65]
	v_cndmask_b32_e64 v53, v228, v63, s[66:67]
	v_cndmask_b32_e64 v64, v228, v64, s[68:69]

.LBB0_655:
	s_and_b64 vcc, exec, s[56:57]
	s_cbranch_vccz .LBB0_786
	v_ashrrev_i32_e32 v0, 31, v192
	v_lshrrev_b32_e32 v0, 26, v0
	v_add_u32_e32 v0, v192, v0
	v_ashrrev_i32_e32 v163, 6, v0
	v_bfe_i32 v0, v192, 27, 1
	v_lshlrev_b32_e32 v177, 4, v192
	v_lshrrev_b32_e32 v0, 22, v0
	v_add_u32_e32 v0, v177, v0
	v_and_b32_e32 v0, 0xfffffc00, v0
	v_sub_u32_e32 v0, v177, v0
	s_waitcnt vmcnt(0)
	v_lshrrev_b32_e32 v2, 4, v0
	v_bitop3_b32 v0, v2, v0, 32 bitop3:0x6c
	v_ashrrev_i32_e32 v3, 31, v0
	v_lshrrev_b32_e32 v3, 26, v3
	v_add_u32_e32 v3, v0, v3
	v_lshlrev_b32_e32 v2, 3, v163
	v_ashrrev_i32_e32 v181, 6, v3
	v_and_b32_e32 v3, 0xc0, v3
	v_and_b32_e32 v2, -16, v2
	v_sub_u32_e32 v0, v0, v3
	v_add_u32_e32 v2, v181, v2
	v_ashrrev_i16_sdwa v0, v225, sext(v0) dst_sel:DWORD dst_unused:UNUSED_PAD src0_sel:DWORD src1_sel:BYTE_0
	v_lshlrev_b32_e32 v4, 5, v163
	v_bfe_i32 v183, v0, 0, 16
	v_lshlrev_b32_e32 v0, 1, v2
	v_lshrrev_b32_e32 v3, 2, v2
	v_and_b32_e32 v5, 3, v181
	s_mov_b32 s4, 0x1fffe0
	v_and_b32_e32 v4, 32, v4
	v_and_b32_e32 v0, 24, v0
	v_and_b32_e32 v3, 4, v3
	v_and_or_b32 v5, v2, s4, v5
	v_or3_b32 v0, v5, v3, v0
	v_add_lshl_u32 v3, v4, v183, 1
	v_lshl_add_u32 v166, v0, 11, v3
	v_add_u32_e32 v0, 0x2000, v177
	v_lshl_add_u32 v164, v2, 11, v3
	v_ashrrev_i32_e32 v2, 31, v0
	v_lshrrev_b32_e32 v2, 22, v2
	v_add_u32_e32 v2, v0, v2
	v_ashrrev_i32_e32 v189, 10, v2
	v_mul_i32_i24_e32 v2, 0x400, v189
	v_sub_u32_e32 v0, v0, v2
	v_lshrrev_b32_e32 v2, 4, v0
	v_bitop3_b32 v0, v2, v0, 32 bitop3:0x6c
	v_ashrrev_i32_e32 v3, 31, v0
	v_lshrrev_b32_e32 v3, 26, v3
	v_add_u32_e32 v3, v0, v3
	v_lshlrev_b32_e32 v2, 3, v189
	v_ashrrev_i32_e32 v193, 6, v3
	v_and_b32_e32 v3, 0xc0, v3
	v_and_b32_e32 v2, -16, v2
	v_sub_u32_e32 v0, v0, v3
	s_load_dwordx2 s[30:31], s[0:1], 0x98
	v_add_u32_e32 v2, v193, v2
	v_ashrrev_i16_sdwa v0, v225, sext(v0) dst_sel:DWORD dst_unused:UNUSED_PAD src0_sel:DWORD src1_sel:BYTE_0
	v_lshlrev_b32_e32 v4, 5, v189
	v_bfe_i32 v195, v0, 0, 16
	v_lshlrev_b32_e32 v0, 1, v2
	v_lshrrev_b32_e32 v3, 2, v2
	v_and_b32_e32 v5, 3, v193
	s_add_i32 s89, s89, 6
	v_and_b32_e32 v4, 32, v4
	v_and_b32_e32 v0, 24, v0
	v_and_b32_e32 v3, 4, v3
	v_and_or_b32 v5, v2, s4, v5
	s_cmp_lt_u32 s89, 15
	v_or3_b32 v0, v5, v3, v0
	v_add_lshl_u32 v3, v4, v195, 1
	v_and_b32_e32 v179, 15, v194
	v_lshlrev_b32_e32 v162, 2, v194
	s_cselect_b64 s[40:41], -1, 0
	v_readfirstlane_b32 s6, v192
	v_lshl_add_u32 v168, v2, 11, v3
	v_lshl_add_u32 v170, v0, 11, v3
	v_lshlrev_b32_e32 v197, 6, v179
	s_cmp_lg_u32 s34, 1
	s_cbranch_scc1 .Les_a_norm
	s_cmp_lg_u32 s100, 0
	s_cbranch_scc1 .Les_a_norm
	v_readlane_b32 s101, v254, 30
	s_cmp_ge_i32 s72, s101
	s_cbranch_scc0 .Les_a_norm
	s_mov_b32 s100, 1
	v_and_b32_e32 v205, 32, v162
	s_branch .LBB0_688
.Les_a_norm:
	s_cmpk_gt_i32 s72, 0x1ff
	v_and_b32_e32 v205, 32, v162
	s_cbranch_scc1 .LBB0_688
	s_ashr_i32 s14, s72, 31
	s_lshr_b32 s4, s14, 29
	s_add_i32 s5, s72, s4
	s_and_b32 s4, s5, -8
	s_sub_i32 s15, s72, s4
	s_cmp_gt_i32 s15, -1
	s_waitcnt lgkmcnt(0)
	s_mov_b64 s[26:27], -1
	s_cbranch_scc0 .LBB0_659
	s_lshl_b32 s4, s15, 6
	s_mov_b64 s[26:27], 0

.LBB0_703:
	s_cmp_lg_u32 s100, 2
	s_cbranch_scc1 .Les_b_norm
	s_mov_b32 s100, 0
	s_branch .LBB0_714

.LBB0_714:
	s_cmp_lg_u32 s100, 1
	s_cbranch_scc1 .Les_c_norm
	s_mov_b32 s100, 2
	s_waitcnt vmcnt(0)
	s_branch .Les_tramp
